# strategy 9: GEMM K-loop back edge rotated (loop-back barrier becomes loop head, header block moved in front of it), on top of v41
# speedup vs baseline: 1.0035x; 1.0035x over previous
.Lrot_head_0:
	s_barrier
.LBB0_538:
	ds_read_b128 v[0:3], v193
	ds_read_b128 v[8:11], v193 offset:2048
	ds_read_b128 v[4:7], v195
	ds_read_b128 v[12:15], v195 offset:2048
	s_add_u32 s15, s24, 0x80
	s_addc_u32 s23, s25, 0
	s_and_b64 s[26:27], s[26:27], exec
	s_cselect_b32 s29, s19, s23
	s_cselect_b32 s28, s18, s15
	s_cselect_b32 s27, s17, s3
	s_cselect_b32 s26, s16, s2
	v_lshl_add_u64 v[16:17], s[24:25], 0, v[168:169]
	s_add_i32 m0, s47, 0xc000
	ds_read_b128 v[218:221], v192
	ds_read_b128 v[226:229], v192 offset:2048
	ds_read_b128 v[222:225], v194
	ds_read_b128 v[230:233], v194 offset:2048
	ds_read_b128 v[234:237], v192 offset:4096
	ds_read_b128 v[242:245], v192 offset:6144
	ds_read_b128 v[238:241], v194 offset:4096
	ds_read_b128 v[246:249], v194 offset:6144
	global_load_lds_dwordx4 v[16:17], off
	v_lshl_add_u64 v[16:17], s[24:25], 0, v[174:175]
	s_add_i32 m0, s47, 0xe000
	s_nop 0
	global_load_lds_dwordx4 v[16:17], off
	s_waitcnt lgkmcnt(8)
	s_barrier
	s_waitcnt lgkmcnt(0)
	s_setprio 1
	s_waitcnt lgkmcnt(0)
	v_mfma_scale_f32_16x16x128_f8f6f4 v[156:159], v[0:7], v[218:225], v[156:159], v191, v191 op_sel_hi:[0,0,0]
	v_mfma_scale_f32_16x16x128_f8f6f4 v[152:155], v[8:15], v[218:225], v[152:155], v191, v191 op_sel_hi:[0,0,0]
	v_mfma_scale_f32_16x16x128_f8f6f4 v[148:151], v[0:7], v[226:233], v[148:151], v191, v191 op_sel_hi:[0,0,0]
	v_mfma_scale_f32_16x16x128_f8f6f4 v[144:147], v[8:15], v[226:233], v[144:147], v191, v191 op_sel_hi:[0,0,0]
	v_mfma_scale_f32_16x16x128_f8f6f4 v[140:143], v[0:7], v[234:241], v[140:143], v191, v191 op_sel_hi:[0,0,0]
	v_mfma_scale_f32_16x16x128_f8f6f4 v[136:139], v[8:15], v[234:241], v[136:139], v191, v191 op_sel_hi:[0,0,0]
	v_mfma_scale_f32_16x16x128_f8f6f4 v[132:135], v[0:7], v[242:249], v[132:135], v191, v191 op_sel_hi:[0,0,0]
	v_mfma_scale_f32_16x16x128_f8f6f4 v[128:131], v[8:15], v[242:249], v[128:131], v191, v191 op_sel_hi:[0,0,0]
	s_setprio 0
	s_barrier
	s_mov_b32 m0, s30
	v_lshl_add_u64 v[182:183], s[26:27], 0, v[162:163]
	ds_read_b128 v[16:19], v193 offset:16384
	ds_read_b128 v[24:27], v193 offset:18432
	ds_read_b128 v[20:23], v195 offset:16384
	ds_read_b128 v[28:31], v195 offset:18432
	global_load_lds_dwordx4 v[182:183], off
	v_lshl_add_u64 v[184:185], s[26:27], 0, v[164:165]
	s_mov_b32 m0, s46
	s_nop 0
	global_load_lds_dwordx4 v[184:185], off
	s_barrier
	s_waitcnt lgkmcnt(0)
	s_setprio 1
	s_waitcnt lgkmcnt(0)
	v_mfma_scale_f32_16x16x128_f8f6f4 v[92:95], v[16:23], v[218:225], v[92:95], v191, v191 op_sel_hi:[0,0,0]
	v_mfma_scale_f32_16x16x128_f8f6f4 v[88:91], v[24:31], v[218:225], v[88:91], v191, v191 op_sel_hi:[0,0,0]
	v_mfma_scale_f32_16x16x128_f8f6f4 v[84:87], v[16:23], v[226:233], v[84:87], v191, v191 op_sel_hi:[0,0,0]
	v_mfma_scale_f32_16x16x128_f8f6f4 v[80:83], v[24:31], v[226:233], v[80:83], v191, v191 op_sel_hi:[0,0,0]
	v_mfma_scale_f32_16x16x128_f8f6f4 v[76:79], v[16:23], v[234:241], v[76:79], v191, v191 op_sel_hi:[0,0,0]
	v_mfma_scale_f32_16x16x128_f8f6f4 v[72:75], v[24:31], v[234:241], v[72:75], v191, v191 op_sel_hi:[0,0,0]
	v_mfma_scale_f32_16x16x128_f8f6f4 v[68:71], v[16:23], v[242:249], v[68:71], v191, v191 op_sel_hi:[0,0,0]
	v_mfma_scale_f32_16x16x128_f8f6f4 v[64:67], v[24:31], v[242:249], v[64:67], v191, v191 op_sel_hi:[0,0,0]
	s_setprio 0
	s_mov_b32 m0, s47
	s_barrier
	ds_read_b128 v[218:221], v192 offset:16384
	ds_read_b128 v[226:229], v192 offset:18432
	ds_read_b128 v[222:225], v194 offset:16384
	ds_read_b128 v[230:233], v194 offset:18432
	ds_read_b128 v[234:237], v192 offset:20480
	ds_read_b128 v[242:245], v192 offset:22528
	ds_read_b128 v[238:241], v194 offset:20480
	ds_read_b128 v[246:249], v194 offset:22528
	global_load_lds_dwordx4 v172, s[28:29]
	s_mov_b32 m0, s83
	v_mov_b32_e32 v187, v173
	global_load_lds_dwordx4 v186, s[28:29]
	s_barrier
	s_waitcnt lgkmcnt(0)
	v_lshl_add_u64 v[188:189], s[28:29], 0, v[172:173]
	v_lshl_add_u64 v[186:187], s[28:29], 0, v[186:187]
	s_setprio 1
	s_waitcnt lgkmcnt(0)
	v_mfma_scale_f32_16x16x128_f8f6f4 v[124:127], v[0:7], v[218:225], v[124:127], v191, v191 op_sel_hi:[0,0,0]
	v_mfma_scale_f32_16x16x128_f8f6f4 v[120:123], v[8:15], v[218:225], v[120:123], v191, v191 op_sel_hi:[0,0,0]
	v_mfma_scale_f32_16x16x128_f8f6f4 v[116:119], v[0:7], v[226:233], v[116:119], v191, v191 op_sel_hi:[0,0,0]
	v_mfma_scale_f32_16x16x128_f8f6f4 v[112:115], v[8:15], v[226:233], v[112:115], v191, v191 op_sel_hi:[0,0,0]
	v_mfma_scale_f32_16x16x128_f8f6f4 v[108:111], v[0:7], v[234:241], v[108:111], v191, v191 op_sel_hi:[0,0,0]
	v_mfma_scale_f32_16x16x128_f8f6f4 v[104:107], v[8:15], v[234:241], v[104:107], v191, v191 op_sel_hi:[0,0,0]
	v_mfma_scale_f32_16x16x128_f8f6f4 v[100:103], v[0:7], v[242:249], v[100:103], v191, v191 op_sel_hi:[0,0,0]
	v_mfma_scale_f32_16x16x128_f8f6f4 v[96:99], v[8:15], v[242:249], v[96:99], v191, v191 op_sel_hi:[0,0,0]
	s_setprio 0
	s_barrier
	s_add_u32 s72, s26, 0x20000
	s_addc_u32 s73, s27, 0
	s_mov_b32 m0, s82
	v_lshl_add_u64 v[0:1], s[72:73], 0, v[162:163]
	global_load_lds_dwordx4 v[0:1], off
	v_lshl_add_u64 v[0:1], s[72:73], 0, v[164:165]
	s_mov_b32 m0, s80
	s_nop 0
	global_load_lds_dwordx4 v[0:1], off
	s_waitcnt vmcnt(6)
	s_barrier
	s_setprio 1
	v_mfma_scale_f32_16x16x128_f8f6f4 v[60:63], v[16:23], v[218:225], v[60:63], v191, v191 op_sel_hi:[0,0,0]
	v_mfma_scale_f32_16x16x128_f8f6f4 v[56:59], v[24:31], v[218:225], v[56:59], v191, v191 op_sel_hi:[0,0,0]
	v_mfma_scale_f32_16x16x128_f8f6f4 v[52:55], v[16:23], v[226:233], v[52:55], v191, v191 op_sel_hi:[0,0,0]
	v_mfma_scale_f32_16x16x128_f8f6f4 v[48:51], v[24:31], v[226:233], v[48:51], v191, v191 op_sel_hi:[0,0,0]
	v_mfma_scale_f32_16x16x128_f8f6f4 v[44:47], v[16:23], v[234:241], v[44:47], v191, v191 op_sel_hi:[0,0,0]
	v_mfma_scale_f32_16x16x128_f8f6f4 v[40:43], v[24:31], v[234:241], v[40:43], v191, v191 op_sel_hi:[0,0,0]
	v_mfma_scale_f32_16x16x128_f8f6f4 v[36:39], v[16:23], v[242:249], v[36:39], v191, v191 op_sel_hi:[0,0,0]
	v_mfma_scale_f32_16x16x128_f8f6f4 v[32:35], v[24:31], v[242:249], v[32:35], v191, v191 op_sel_hi:[0,0,0]
	s_setprio 0
	s_barrier
	ds_read_b128 v[0:3], v193 offset:32768
	ds_read_b128 v[8:11], v193 offset:34816
	ds_read_b128 v[4:7], v195 offset:32768
	ds_read_b128 v[12:15], v195 offset:34816
	s_mov_b32 m0, s81
	v_lshl_add_u64 v[180:181], s[28:29], 0, v[180:181]
	ds_read_b128 v[16:19], v192 offset:32768
	ds_read_b128 v[24:27], v192 offset:34816
	ds_read_b128 v[20:23], v194 offset:32768
	ds_read_b128 v[28:31], v194 offset:34816
	ds_read_b128 v[218:221], v192 offset:36864
	ds_read_b128 v[226:229], v192 offset:38912
	ds_read_b128 v[222:225], v194 offset:36864
	ds_read_b128 v[230:233], v194 offset:38912
	global_load_lds_dwordx4 v[180:181], off
	v_lshl_add_u64 v[178:179], s[28:29], 0, v[178:179]
	s_mov_b32 m0, s50
	s_nop 0
	global_load_lds_dwordx4 v[178:179], off
	s_waitcnt lgkmcnt(8)
	s_barrier
	s_waitcnt lgkmcnt(0)
	s_setprio 1
	s_waitcnt lgkmcnt(0)
	v_mfma_scale_f32_16x16x128_f8f6f4 v[156:159], v[0:7], v[16:23], v[156:159], v191, v191 op_sel_hi:[0,0,0]
	v_mfma_scale_f32_16x16x128_f8f6f4 v[152:155], v[8:15], v[16:23], v[152:155], v191, v191 op_sel_hi:[0,0,0]
	v_mfma_scale_f32_16x16x128_f8f6f4 v[148:151], v[0:7], v[24:31], v[148:151], v191, v191 op_sel_hi:[0,0,0]
	v_mfma_scale_f32_16x16x128_f8f6f4 v[144:147], v[8:15], v[24:31], v[144:147], v191, v191 op_sel_hi:[0,0,0]
	v_mfma_scale_f32_16x16x128_f8f6f4 v[140:143], v[0:7], v[218:225], v[140:143], v191, v191 op_sel_hi:[0,0,0]
	v_mfma_scale_f32_16x16x128_f8f6f4 v[136:139], v[8:15], v[218:225], v[136:139], v191, v191 op_sel_hi:[0,0,0]
	v_mfma_scale_f32_16x16x128_f8f6f4 v[132:135], v[0:7], v[226:233], v[132:135], v191, v191 op_sel_hi:[0,0,0]
	v_mfma_scale_f32_16x16x128_f8f6f4 v[128:131], v[8:15], v[226:233], v[128:131], v191, v191 op_sel_hi:[0,0,0]
	s_setprio 0
	s_barrier
	s_mov_b32 m0, s51
	v_lshl_add_u64 v[178:179], v[182:183], 0, s[40:41]
	ds_read_b128 v[234:237], v193 offset:49152
	ds_read_b128 v[242:245], v193 offset:51200
	ds_read_b128 v[238:241], v195 offset:49152
	ds_read_b128 v[246:249], v195 offset:51200
	global_load_lds_dwordx4 v[178:179], off
	v_lshl_add_u64 v[178:179], v[184:185], 0, s[40:41]
	s_mov_b32 m0, s70
	s_nop 0
	global_load_lds_dwordx4 v[178:179], off
	s_barrier
	s_waitcnt lgkmcnt(0)
	s_setprio 1
	s_waitcnt lgkmcnt(0)
	v_mfma_scale_f32_16x16x128_f8f6f4 v[92:95], v[234:241], v[16:23], v[92:95], v191, v191 op_sel_hi:[0,0,0]
	v_mfma_scale_f32_16x16x128_f8f6f4 v[88:91], v[242:249], v[16:23], v[88:91], v191, v191 op_sel_hi:[0,0,0]
	v_mfma_scale_f32_16x16x128_f8f6f4 v[84:87], v[234:241], v[24:31], v[84:87], v191, v191 op_sel_hi:[0,0,0]
	v_mfma_scale_f32_16x16x128_f8f6f4 v[80:83], v[242:249], v[24:31], v[80:83], v191, v191 op_sel_hi:[0,0,0]
	v_mfma_scale_f32_16x16x128_f8f6f4 v[76:79], v[234:241], v[218:225], v[76:79], v191, v191 op_sel_hi:[0,0,0]
	v_mfma_scale_f32_16x16x128_f8f6f4 v[72:75], v[242:249], v[218:225], v[72:75], v191, v191 op_sel_hi:[0,0,0]
	v_mfma_scale_f32_16x16x128_f8f6f4 v[68:71], v[234:241], v[226:233], v[68:71], v191, v191 op_sel_hi:[0,0,0]
	v_mfma_scale_f32_16x16x128_f8f6f4 v[64:67], v[242:249], v[226:233], v[64:67], v191, v191 op_sel_hi:[0,0,0]
	s_setprio 0
	s_mov_b32 m0, s71
	v_lshl_add_u64 v[188:189], v[188:189], 0, s[40:41]
	s_barrier
	ds_read_b128 v[16:19], v192 offset:49152
	ds_read_b128 v[24:27], v192 offset:51200
	ds_read_b128 v[20:23], v194 offset:49152
	ds_read_b128 v[28:31], v194 offset:51200
	ds_read_b128 v[178:181], v192 offset:53248
	ds_read_b128 v[218:221], v192 offset:55296
	ds_read_b128 v[182:185], v194 offset:53248
	ds_read_b128 v[222:225], v194 offset:55296
	global_load_lds_dwordx4 v[188:189], off
	v_lshl_add_u64 v[186:187], v[186:187], 0, s[40:41]
	s_mov_b32 m0, s87
	s_nop 0
	global_load_lds_dwordx4 v[186:187], off
	s_barrier
	s_waitcnt lgkmcnt(0)
	s_setprio 1
	s_waitcnt lgkmcnt(0)
	v_mfma_scale_f32_16x16x128_f8f6f4 v[124:127], v[0:7], v[16:23], v[124:127], v191, v191 op_sel_hi:[0,0,0]
	v_mfma_scale_f32_16x16x128_f8f6f4 v[120:123], v[8:15], v[16:23], v[120:123], v191, v191 op_sel_hi:[0,0,0]
	v_mfma_scale_f32_16x16x128_f8f6f4 v[116:119], v[0:7], v[24:31], v[116:119], v191, v191 op_sel_hi:[0,0,0]
	v_mfma_scale_f32_16x16x128_f8f6f4 v[112:115], v[8:15], v[24:31], v[112:115], v191, v191 op_sel_hi:[0,0,0]
	v_mfma_scale_f32_16x16x128_f8f6f4 v[108:111], v[0:7], v[178:185], v[108:111], v191, v191 op_sel_hi:[0,0,0]
	v_mfma_scale_f32_16x16x128_f8f6f4 v[104:107], v[8:15], v[178:185], v[104:107], v191, v191 op_sel_hi:[0,0,0]
	v_mfma_scale_f32_16x16x128_f8f6f4 v[100:103], v[0:7], v[218:225], v[100:103], v191, v191 op_sel_hi:[0,0,0]
	v_mfma_scale_f32_16x16x128_f8f6f4 v[96:99], v[8:15], v[218:225], v[96:99], v191, v191 op_sel_hi:[0,0,0]
	s_setprio 0
	s_barrier
	s_add_u32 s26, s26, 0x20080
	s_addc_u32 s27, s27, 0
	s_mov_b32 m0, s1
	v_lshl_add_u64 v[0:1], s[26:27], 0, v[162:163]
	global_load_lds_dwordx4 v[0:1], off
	v_lshl_add_u64 v[0:1], s[26:27], 0, v[164:165]
	s_mov_b32 m0, s56
	s_nop 0
	global_load_lds_dwordx4 v[0:1], off
	s_waitcnt vmcnt(6)
	s_barrier
	s_setprio 1
	v_mfma_scale_f32_16x16x128_f8f6f4 v[60:63], v[234:241], v[16:23], v[60:63], v191, v191 op_sel_hi:[0,0,0]
	v_mfma_scale_f32_16x16x128_f8f6f4 v[56:59], v[242:249], v[16:23], v[56:59], v191, v191 op_sel_hi:[0,0,0]
	v_mfma_scale_f32_16x16x128_f8f6f4 v[52:55], v[234:241], v[24:31], v[52:55], v191, v191 op_sel_hi:[0,0,0]
	v_mfma_scale_f32_16x16x128_f8f6f4 v[48:51], v[242:249], v[24:31], v[48:51], v191, v191 op_sel_hi:[0,0,0]
	v_mfma_scale_f32_16x16x128_f8f6f4 v[44:47], v[234:241], v[178:185], v[44:47], v191, v191 op_sel_hi:[0,0,0]
	v_mfma_scale_f32_16x16x128_f8f6f4 v[40:43], v[242:249], v[178:185], v[40:43], v191, v191 op_sel_hi:[0,0,0]
	v_mfma_scale_f32_16x16x128_f8f6f4 v[36:39], v[234:241], v[218:225], v[36:39], v191, v191 op_sel_hi:[0,0,0]
	v_mfma_scale_f32_16x16x128_f8f6f4 v[32:35], v[242:249], v[218:225], v[32:35], v191, v191 op_sel_hi:[0,0,0]
	s_setprio 0
	s_add_i32 s13, s13, 2
	s_add_u32 s24, s24, 0x100
	s_addc_u32 s25, s25, 0
	s_add_u32 s2, s2, 0x100
	s_addc_u32 s3, s3, 0
	s_cmp_gt_u32 s13, 5
	s_cbranch_scc1 .Lrot_exit_0
	s_cmp_eq_u32 s13, 4
	s_cselect_b64 s[26:27], -1, 0
	s_cmp_lg_u32 s13, 4
	v_mov_b64_e32 v[178:179], v[174:175]
	v_mov_b64_e32 v[180:181], v[168:169]
	v_mov_b32_e32 v186, v176
	v_mov_b32_e32 v172, v170
	s_cbranch_scc1 .Lrot_head_0
	v_mov_b32_e32 v178, v217
	v_mov_b32_e32 v0, v214
	v_mov_b32_e32 v172, v215
	v_mov_b32_e32 v186, v216
	v_mov_b32_e32 v179, v173
	v_mov_b64_e32 v[180:181], v[172:173]
	v_mov_b32_e32 v172, v0
	s_branch .Lrot_head_0
.Lrot_exit_0:
	s_barrier
	s_branch .LBB0_541

.LBB0_1319:
	ds_read_b128 v[142:145], v186
	ds_read_b128 v[146:149], v186 offset:1024
	ds_read_b128 v[150:153], v186 offset:2048
	ds_read_b128 v[162:165], v186 offset:3072
	s_add_u32 s30, s26, 0x80
	s_addc_u32 s31, s27, 0
	s_and_b64 s[28:29], s[28:29], exec
	s_cselect_b32 s31, s19, s31
	s_cselect_b32 s30, s18, s30
	s_cselect_b32 s29, s17, s15
	s_cselect_b32 s28, s16, s9
	v_lshl_add_u64 v[154:155], s[26:27], 0, v[128:129]
	s_add_i32 m0, s23, 0xc000
	ds_read_b128 v[166:169], v185
	ds_read_b128 v[174:177], v185 offset:1024
	ds_read_b128 v[178:181], v185 offset:2048
	ds_read_b128 v[204:207], v185 offset:3072
	ds_read_b128 v[208:211], v185 offset:4096
	ds_read_b128 v[214:217], v185 offset:5120
	ds_read_b128 v[218:221], v185 offset:6144
	ds_read_b128 v[222:225], v185 offset:7168
	global_load_lds_dwordx4 v[154:155], off
	v_lshl_add_u64 v[154:155], s[26:27], 0, v[132:133]
	s_add_i32 m0, s23, 0xe000
	s_nop 0
	global_load_lds_dwordx4 v[154:155], off
	s_waitcnt lgkmcnt(8)
	s_barrier
	s_waitcnt lgkmcnt(0)
	s_setprio 1
	s_waitcnt lgkmcnt(0)
	v_mfma_f32_16x16x32_bf16 v[124:127], v[142:145], v[166:169], v[124:127]
	v_mfma_f32_16x16x32_bf16 v[120:123], v[150:153], v[166:169], v[120:123]
	v_mfma_f32_16x16x32_bf16 v[116:119], v[142:145], v[178:181], v[116:119]
	v_mfma_f32_16x16x32_bf16 v[112:115], v[150:153], v[178:181], v[112:115]
	v_mfma_f32_16x16x32_bf16 v[108:111], v[142:145], v[208:211], v[108:111]
	v_mfma_f32_16x16x32_bf16 v[104:107], v[150:153], v[208:211], v[104:107]
	v_mfma_f32_16x16x32_bf16 v[100:103], v[142:145], v[218:221], v[100:103]
	v_mfma_f32_16x16x32_bf16 v[96:99], v[150:153], v[218:221], v[96:99]
	v_mfma_f32_16x16x32_bf16 v[124:127], v[146:149], v[174:177], v[124:127]
	v_mfma_f32_16x16x32_bf16 v[120:123], v[162:165], v[174:177], v[120:123]
	v_mfma_f32_16x16x32_bf16 v[116:119], v[146:149], v[204:207], v[116:119]
	v_mfma_f32_16x16x32_bf16 v[112:115], v[162:165], v[204:207], v[112:115]
	v_mfma_f32_16x16x32_bf16 v[108:111], v[146:149], v[214:217], v[108:111]
	v_mfma_f32_16x16x32_bf16 v[104:107], v[162:165], v[214:217], v[104:107]
	v_mfma_f32_16x16x32_bf16 v[100:103], v[146:149], v[222:225], v[100:103]
	v_mfma_f32_16x16x32_bf16 v[96:99], v[162:165], v[222:225], v[96:99]
	s_setprio 0
	s_barrier
	s_mov_b32 m0, s25
	v_lshl_add_u64 v[170:171], s[28:29], 0, v[158:159]
	ds_read_b128 v[226:229], v186 offset:16384
	ds_read_b128 v[230:233], v186 offset:17408
	ds_read_b128 v[234:237], v186 offset:18432
	ds_read_b128 v[238:241], v186 offset:19456
	global_load_lds_dwordx4 v[170:171], off
	v_lshl_add_u64 v[182:183], s[28:29], 0, v[160:161]
	s_mov_b32 m0, s51
	s_nop 0
	global_load_lds_dwordx4 v[182:183], off
	s_barrier
	s_waitcnt lgkmcnt(0)
	s_setprio 1
	s_waitcnt lgkmcnt(0)
	v_mfma_f32_16x16x32_bf16 v[68:71], v[226:229], v[166:169], v[68:71]
	v_mfma_f32_16x16x32_bf16 v[64:67], v[234:237], v[166:169], v[64:67]
	v_mfma_f32_16x16x32_bf16 v[52:55], v[226:229], v[178:181], v[52:55]
	v_mfma_f32_16x16x32_bf16 v[48:51], v[234:237], v[178:181], v[48:51]
	v_mfma_f32_16x16x32_bf16 v[44:47], v[226:229], v[208:211], v[44:47]
	v_mfma_f32_16x16x32_bf16 v[40:43], v[234:237], v[208:211], v[40:43]
	v_mfma_f32_16x16x32_bf16 v[36:39], v[226:229], v[218:221], v[36:39]
	v_mfma_f32_16x16x32_bf16 v[32:35], v[234:237], v[218:221], v[32:35]
	v_mfma_f32_16x16x32_bf16 v[68:71], v[230:233], v[174:177], v[68:71]
	v_mfma_f32_16x16x32_bf16 v[64:67], v[238:241], v[174:177], v[64:67]
	v_mfma_f32_16x16x32_bf16 v[52:55], v[230:233], v[204:207], v[52:55]
	v_mfma_f32_16x16x32_bf16 v[48:51], v[238:241], v[204:207], v[48:51]
	v_mfma_f32_16x16x32_bf16 v[44:47], v[230:233], v[214:217], v[44:47]
	v_mfma_f32_16x16x32_bf16 v[40:43], v[238:241], v[214:217], v[40:43]
	v_mfma_f32_16x16x32_bf16 v[36:39], v[230:233], v[222:225], v[36:39]
	v_mfma_f32_16x16x32_bf16 v[32:35], v[238:241], v[222:225], v[32:35]
	s_setprio 0
	s_mov_b32 m0, s23
	s_barrier
	ds_read_b128 v[166:169], v185 offset:16384
	ds_read_b128 v[174:177], v185 offset:17408
	ds_read_b128 v[178:181], v185 offset:18432
	ds_read_b128 v[204:207], v185 offset:19456
	ds_read_b128 v[208:211], v185 offset:20480
	ds_read_b128 v[214:217], v185 offset:21504
	ds_read_b128 v[218:221], v185 offset:22528
	ds_read_b128 v[222:225], v185 offset:23552
	global_load_lds_dwordx4 v172, s[30:31]
	s_mov_b32 m0, s56
	v_mov_b32_e32 v141, v173
	global_load_lds_dwordx4 v140, s[30:31]
	s_barrier
	s_waitcnt lgkmcnt(0)
	v_lshl_add_u64 v[196:197], s[30:31], 0, v[172:173]
	v_lshl_add_u64 v[242:243], s[30:31], 0, v[140:141]
	s_setprio 1
	s_waitcnt lgkmcnt(0)
	v_mfma_f32_16x16x32_bf16 v[92:95], v[142:145], v[166:169], v[92:95]
	v_mfma_f32_16x16x32_bf16 v[88:91], v[150:153], v[166:169], v[88:91]
	v_mfma_f32_16x16x32_bf16 v[84:87], v[142:145], v[178:181], v[84:87]
	v_mfma_f32_16x16x32_bf16 v[80:83], v[150:153], v[178:181], v[80:83]
	v_mfma_f32_16x16x32_bf16 v[76:79], v[142:145], v[208:211], v[76:79]
	v_mfma_f32_16x16x32_bf16 v[72:75], v[150:153], v[208:211], v[72:75]
	v_mfma_f32_16x16x32_bf16 v[60:63], v[142:145], v[218:221], v[60:63]
	v_mfma_f32_16x16x32_bf16 v[56:59], v[150:153], v[218:221], v[56:59]
	v_mfma_f32_16x16x32_bf16 v[92:95], v[146:149], v[174:177], v[92:95]
	v_mfma_f32_16x16x32_bf16 v[88:91], v[162:165], v[174:177], v[88:91]
	v_mfma_f32_16x16x32_bf16 v[84:87], v[146:149], v[204:207], v[84:87]
	v_mfma_f32_16x16x32_bf16 v[80:83], v[162:165], v[204:207], v[80:83]
	v_mfma_f32_16x16x32_bf16 v[76:79], v[146:149], v[214:217], v[76:79]
	v_mfma_f32_16x16x32_bf16 v[72:75], v[162:165], v[214:217], v[72:75]
	v_mfma_f32_16x16x32_bf16 v[60:63], v[146:149], v[222:225], v[60:63]
	v_mfma_f32_16x16x32_bf16 v[56:59], v[162:165], v[222:225], v[56:59]
	s_setprio 0
	s_barrier
	s_add_u32 s94, s28, 0x40000
	s_addc_u32 s95, s29, 0
	s_mov_b32 m0, s65
	v_lshl_add_u64 v[140:141], s[94:95], 0, v[158:159]
	global_load_lds_dwordx4 v[140:141], off
	v_lshl_add_u64 v[140:141], s[94:95], 0, v[160:161]
	s_mov_b32 m0, s70
	s_nop 0
	global_load_lds_dwordx4 v[140:141], off
	s_waitcnt vmcnt(6)
	s_barrier
	s_setprio 1
	v_mfma_f32_16x16x32_bf16 v[28:31], v[226:229], v[166:169], v[28:31]
	v_mfma_f32_16x16x32_bf16 v[24:27], v[234:237], v[166:169], v[24:27]
	v_mfma_f32_16x16x32_bf16 v[20:23], v[226:229], v[178:181], v[20:23]
	v_mfma_f32_16x16x32_bf16 v[16:19], v[234:237], v[178:181], v[16:19]
	v_mfma_f32_16x16x32_bf16 v[12:15], v[226:229], v[208:211], v[12:15]
	v_mfma_f32_16x16x32_bf16 v[8:11], v[234:237], v[208:211], v[8:11]
	v_mfma_f32_16x16x32_bf16 v[4:7], v[226:229], v[218:221], v[4:7]
	v_mfma_f32_16x16x32_bf16 v[0:3], v[234:237], v[218:221], v[0:3]
	v_mfma_f32_16x16x32_bf16 v[28:31], v[230:233], v[174:177], v[28:31]
	v_mfma_f32_16x16x32_bf16 v[24:27], v[238:241], v[174:177], v[24:27]
	v_mfma_f32_16x16x32_bf16 v[20:23], v[230:233], v[204:207], v[20:23]
	v_mfma_f32_16x16x32_bf16 v[16:19], v[238:241], v[204:207], v[16:19]
	v_mfma_f32_16x16x32_bf16 v[12:15], v[230:233], v[214:217], v[12:15]
	v_mfma_f32_16x16x32_bf16 v[8:11], v[238:241], v[214:217], v[8:11]
	v_mfma_f32_16x16x32_bf16 v[4:7], v[230:233], v[222:225], v[4:7]
	v_mfma_f32_16x16x32_bf16 v[0:3], v[238:241], v[222:225], v[0:3]
	s_setprio 0
	s_barrier
	ds_read_b128 v[140:143], v186 offset:32768
	ds_read_b128 v[144:147], v186 offset:33792
	ds_read_b128 v[148:151], v186 offset:34816
	ds_read_b128 v[152:155], v186 offset:35840
	s_mov_b32 m0, s71
	v_lshl_add_u64 v[138:139], s[30:31], 0, v[138:139]
	ds_read_b128 v[162:165], v185 offset:32768
	ds_read_b128 v[166:169], v185 offset:33792
	ds_read_b128 v[174:177], v185 offset:34816
	ds_read_b128 v[178:181], v185 offset:35840
	ds_read_b128 v[204:207], v185 offset:36864
	ds_read_b128 v[208:211], v185 offset:37888
	ds_read_b128 v[214:217], v185 offset:38912
	ds_read_b128 v[218:221], v185 offset:39936
	global_load_lds_dwordx4 v[138:139], off
	v_lshl_add_u64 v[136:137], s[30:31], 0, v[136:137]
	s_mov_b32 m0, s80
	s_nop 0
	global_load_lds_dwordx4 v[136:137], off
	s_waitcnt lgkmcnt(8)
	s_barrier
	s_waitcnt lgkmcnt(0)
	s_setprio 1
	s_waitcnt lgkmcnt(0)
	v_mfma_f32_16x16x32_bf16 v[124:127], v[140:143], v[162:165], v[124:127]
	v_mfma_f32_16x16x32_bf16 v[120:123], v[148:151], v[162:165], v[120:123]
	v_mfma_f32_16x16x32_bf16 v[116:119], v[140:143], v[174:177], v[116:119]
	v_mfma_f32_16x16x32_bf16 v[112:115], v[148:151], v[174:177], v[112:115]
	v_mfma_f32_16x16x32_bf16 v[108:111], v[140:143], v[204:207], v[108:111]
	v_mfma_f32_16x16x32_bf16 v[104:107], v[148:151], v[204:207], v[104:107]
	v_mfma_f32_16x16x32_bf16 v[100:103], v[140:143], v[214:217], v[100:103]
	v_mfma_f32_16x16x32_bf16 v[96:99], v[148:151], v[214:217], v[96:99]
	v_mfma_f32_16x16x32_bf16 v[124:127], v[144:147], v[166:169], v[124:127]
	v_mfma_f32_16x16x32_bf16 v[120:123], v[152:155], v[166:169], v[120:123]
	v_mfma_f32_16x16x32_bf16 v[116:119], v[144:147], v[178:181], v[116:119]
	v_mfma_f32_16x16x32_bf16 v[112:115], v[152:155], v[178:181], v[112:115]
	v_mfma_f32_16x16x32_bf16 v[108:111], v[144:147], v[208:211], v[108:111]
	v_mfma_f32_16x16x32_bf16 v[104:107], v[152:155], v[208:211], v[104:107]
	v_mfma_f32_16x16x32_bf16 v[100:103], v[144:147], v[218:221], v[100:103]
	v_mfma_f32_16x16x32_bf16 v[96:99], v[152:155], v[218:221], v[96:99]
	s_setprio 0
	s_barrier
	s_mov_b32 m0, s81
	v_lshl_add_u64 v[170:171], v[170:171], 0, s[40:41]
	ds_read_b128 v[136:139], v186 offset:49152
	ds_read_b128 v[222:225], v186 offset:50176
	ds_read_b128 v[226:229], v186 offset:51200
	ds_read_b128 v[230:233], v186 offset:52224
	global_load_lds_dwordx4 v[170:171], off
	v_lshl_add_u64 v[170:171], v[182:183], 0, s[40:41]
	s_mov_b32 m0, s82
	s_nop 0
	global_load_lds_dwordx4 v[170:171], off
	s_barrier
	s_waitcnt lgkmcnt(0)
	s_setprio 1
	s_waitcnt lgkmcnt(0)
	v_mfma_f32_16x16x32_bf16 v[68:71], v[136:139], v[162:165], v[68:71]
	v_mfma_f32_16x16x32_bf16 v[64:67], v[226:229], v[162:165], v[64:67]
	v_mfma_f32_16x16x32_bf16 v[52:55], v[136:139], v[174:177], v[52:55]
	v_mfma_f32_16x16x32_bf16 v[48:51], v[226:229], v[174:177], v[48:51]
	v_mfma_f32_16x16x32_bf16 v[44:47], v[136:139], v[204:207], v[44:47]
	v_mfma_f32_16x16x32_bf16 v[40:43], v[226:229], v[204:207], v[40:43]
	v_mfma_f32_16x16x32_bf16 v[36:39], v[136:139], v[214:217], v[36:39]
	v_mfma_f32_16x16x32_bf16 v[32:35], v[226:229], v[214:217], v[32:35]
	v_mfma_f32_16x16x32_bf16 v[68:71], v[222:225], v[166:169], v[68:71]
	v_mfma_f32_16x16x32_bf16 v[64:67], v[230:233], v[166:169], v[64:67]
	v_mfma_f32_16x16x32_bf16 v[52:55], v[222:225], v[178:181], v[52:55]
	v_mfma_f32_16x16x32_bf16 v[48:51], v[230:233], v[178:181], v[48:51]
	v_mfma_f32_16x16x32_bf16 v[44:47], v[222:225], v[208:211], v[44:47]
	v_mfma_f32_16x16x32_bf16 v[40:43], v[230:233], v[208:211], v[40:43]
	v_mfma_f32_16x16x32_bf16 v[36:39], v[222:225], v[218:221], v[36:39]
	v_mfma_f32_16x16x32_bf16 v[32:35], v[230:233], v[218:221], v[32:35]
	s_setprio 0
	s_mov_b32 m0, s83
	v_lshl_add_u64 v[170:171], v[196:197], 0, s[40:41]
	s_barrier
	ds_read_b128 v[162:165], v185 offset:49152
	ds_read_b128 v[166:169], v185 offset:50176
	ds_read_b128 v[174:177], v185 offset:51200
	ds_read_b128 v[178:181], v185 offset:52224
	ds_read_b128 v[204:207], v185 offset:53248
	ds_read_b128 v[208:211], v185 offset:54272
	ds_read_b128 v[214:217], v185 offset:55296
	ds_read_b128 v[218:221], v185 offset:56320
	global_load_lds_dwordx4 v[170:171], off
	v_lshl_add_u64 v[170:171], v[242:243], 0, s[40:41]
	s_mov_b32 m0, s85
	s_nop 0
	global_load_lds_dwordx4 v[170:171], off
	s_barrier
	s_waitcnt lgkmcnt(0)
	s_setprio 1
	s_waitcnt lgkmcnt(0)
	v_mfma_f32_16x16x32_bf16 v[92:95], v[140:143], v[162:165], v[92:95]
	v_mfma_f32_16x16x32_bf16 v[88:91], v[148:151], v[162:165], v[88:91]
	v_mfma_f32_16x16x32_bf16 v[84:87], v[140:143], v[174:177], v[84:87]
	v_mfma_f32_16x16x32_bf16 v[80:83], v[148:151], v[174:177], v[80:83]
	v_mfma_f32_16x16x32_bf16 v[76:79], v[140:143], v[204:207], v[76:79]
	v_mfma_f32_16x16x32_bf16 v[72:75], v[148:151], v[204:207], v[72:75]
	v_mfma_f32_16x16x32_bf16 v[60:63], v[140:143], v[214:217], v[60:63]
	v_mfma_f32_16x16x32_bf16 v[56:59], v[148:151], v[214:217], v[56:59]
	v_mfma_f32_16x16x32_bf16 v[92:95], v[144:147], v[166:169], v[92:95]
	v_mfma_f32_16x16x32_bf16 v[88:91], v[152:155], v[166:169], v[88:91]
	v_mfma_f32_16x16x32_bf16 v[84:87], v[144:147], v[178:181], v[84:87]
	v_mfma_f32_16x16x32_bf16 v[80:83], v[152:155], v[178:181], v[80:83]
	v_mfma_f32_16x16x32_bf16 v[76:79], v[144:147], v[208:211], v[76:79]
	v_mfma_f32_16x16x32_bf16 v[72:75], v[152:155], v[208:211], v[72:75]
	v_mfma_f32_16x16x32_bf16 v[60:63], v[144:147], v[218:221], v[60:63]
	v_mfma_f32_16x16x32_bf16 v[56:59], v[152:155], v[218:221], v[56:59]
	s_setprio 0
	s_barrier
	s_add_u32 s28, s28, 0x40080
	s_addc_u32 s29, s29, 0
	s_mov_b32 m0, s87
	v_lshl_add_u64 v[140:141], s[28:29], 0, v[158:159]
	global_load_lds_dwordx4 v[140:141], off
	v_lshl_add_u64 v[140:141], s[28:29], 0, v[160:161]
	s_mov_b32 m0, s44
	s_nop 0
	global_load_lds_dwordx4 v[140:141], off
	s_waitcnt vmcnt(6)
	s_barrier
	s_setprio 1
	v_mfma_f32_16x16x32_bf16 v[28:31], v[136:139], v[162:165], v[28:31]
	v_mfma_f32_16x16x32_bf16 v[24:27], v[226:229], v[162:165], v[24:27]
	v_mfma_f32_16x16x32_bf16 v[20:23], v[136:139], v[174:177], v[20:23]
	v_mfma_f32_16x16x32_bf16 v[16:19], v[226:229], v[174:177], v[16:19]
	v_mfma_f32_16x16x32_bf16 v[12:15], v[136:139], v[204:207], v[12:15]
	v_mfma_f32_16x16x32_bf16 v[8:11], v[226:229], v[204:207], v[8:11]
	v_mfma_f32_16x16x32_bf16 v[4:7], v[136:139], v[214:217], v[4:7]
	v_mfma_f32_16x16x32_bf16 v[0:3], v[226:229], v[214:217], v[0:3]
	v_mfma_f32_16x16x32_bf16 v[28:31], v[222:225], v[166:169], v[28:31]
	v_mfma_f32_16x16x32_bf16 v[24:27], v[230:233], v[166:169], v[24:27]
	v_mfma_f32_16x16x32_bf16 v[20:23], v[222:225], v[178:181], v[20:23]
	v_mfma_f32_16x16x32_bf16 v[16:19], v[230:233], v[178:181], v[16:19]
	v_mfma_f32_16x16x32_bf16 v[12:15], v[222:225], v[208:211], v[12:15]
	v_mfma_f32_16x16x32_bf16 v[8:11], v[230:233], v[208:211], v[8:11]
	v_mfma_f32_16x16x32_bf16 v[4:7], v[222:225], v[218:221], v[4:7]
	v_mfma_f32_16x16x32_bf16 v[0:3], v[230:233], v[218:221], v[0:3]
	s_setprio 0
	s_add_i32 vcc_lo, vcc_lo, 2
	s_add_u32 s26, s26, 0x100
	s_addc_u32 s27, s27, 0
	s_add_u32 s9, s9, 0x100
	s_addc_u32 s15, s15, 0
	s_cmp_gt_u32 vcc_lo, 13
	s_cbranch_scc1 .Lrot_exit_1
	s_cmp_eq_u32 vcc_lo, 12
	s_cselect_b64 s[28:29], -1, 0
	s_cmp_lg_u32 vcc_lo, 12
	v_mov_b64_e32 v[136:137], v[132:133]
	v_mov_b64_e32 v[138:139], v[128:129]
	v_mov_b32_e32 v172, v130
	v_mov_b32_e32 v140, v134
	s_cbranch_scc1 .Lrot_head_1
	v_mov_b32_e32 v136, v195
	v_mov_b32_e32 v131, v192
	v_mov_b32_e32 v172, v193
	v_mov_b32_e32 v140, v194
	v_mov_b32_e32 v137, v173
	v_mov_b64_e32 v[138:139], v[172:173]
	v_mov_b32_e32 v172, v131
	s_branch .Lrot_head_1

.LBB0_1554:
	v_mov_b32_e32 v186, v166
	v_mov_b32_e32 v184, v170
	v_mov_b64_e32 v[178:179], v[168:169]
	v_mov_b64_e32 v[176:177], v[174:175]
	s_branch .LBB0_1555

.LBB0_1555:
	ds_read_b128 v[0:3], v191
	ds_read_b128 v[8:11], v191 offset:2048
	ds_read_b128 v[4:7], v193
	ds_read_b128 v[12:15], v193 offset:2048
	s_add_u32 s26, s22, 0x80
	s_addc_u32 s27, s23, 0
	s_and_b64 s[24:25], s[24:25], exec
	s_cselect_b32 s27, s19, s27
	s_cselect_b32 s26, s18, s26
	s_cselect_b32 s25, s17, s3
	s_cselect_b32 s24, s16, s2
	v_lshl_add_u64 v[16:17], s[22:23], 0, v[168:169]
	s_add_i32 m0, s44, 0xc000
	ds_read_b128 v[226:229], v190
	ds_read_b128 v[234:237], v190 offset:2048
	ds_read_b128 v[230:233], v192
	ds_read_b128 v[238:241], v192 offset:2048
	ds_read_b128 v[242:245], v190 offset:4096
	ds_read_b128 v[204:207], v190 offset:6144
	ds_read_b128 v[246:249], v192 offset:4096
	ds_read_b128 v[208:211], v192 offset:6144
	global_load_lds_dwordx4 v[16:17], off
	v_lshl_add_u64 v[16:17], s[22:23], 0, v[174:175]
	s_add_i32 m0, s44, 0xe000
	s_nop 0
	global_load_lds_dwordx4 v[16:17], off
	s_waitcnt lgkmcnt(8)
	s_barrier
	s_waitcnt lgkmcnt(0)
	s_setprio 1
	s_waitcnt lgkmcnt(0)
	v_mfma_scale_f32_16x16x128_f8f6f4 v[156:159], v[0:7], v[226:233], v[156:159], v189, v189 op_sel_hi:[0,0,0]
	v_mfma_scale_f32_16x16x128_f8f6f4 v[148:151], v[8:15], v[226:233], v[148:151], v189, v189 op_sel_hi:[0,0,0]
	v_mfma_scale_f32_16x16x128_f8f6f4 v[140:143], v[0:7], v[234:241], v[140:143], v189, v189 op_sel_hi:[0,0,0]
	v_mfma_scale_f32_16x16x128_f8f6f4 v[132:135], v[8:15], v[234:241], v[132:135], v189, v189 op_sel_hi:[0,0,0]
	v_mfma_scale_f32_16x16x128_f8f6f4 v[124:127], v[0:7], v[242:249], v[124:127], v189, v189 op_sel_hi:[0,0,0]
	v_mfma_scale_f32_16x16x128_f8f6f4 v[116:119], v[8:15], v[242:249], v[116:119], v189, v189 op_sel_hi:[0,0,0]
	v_mfma_scale_f32_16x16x128_f8f6f4 v[108:111], v[0:7], v[204:211], v[108:111], v189, v189 op_sel_hi:[0,0,0]
	v_mfma_scale_f32_16x16x128_f8f6f4 v[100:103], v[8:15], v[204:211], v[100:103], v189, v189 op_sel_hi:[0,0,0]
	s_setprio 0
	s_barrier
	s_mov_b32 m0, s46
	v_lshl_add_u64 v[180:181], s[24:25], 0, v[160:161]
	ds_read_b128 v[16:19], v191 offset:16384
	ds_read_b128 v[24:27], v191 offset:18432
	ds_read_b128 v[20:23], v193 offset:16384
	ds_read_b128 v[28:31], v193 offset:18432
	global_load_lds_dwordx4 v[180:181], off
	v_lshl_add_u64 v[182:183], s[24:25], 0, v[162:163]
	s_mov_b32 m0, s47
	s_nop 0
	global_load_lds_dwordx4 v[182:183], off
	s_barrier
	s_waitcnt lgkmcnt(0)
	s_setprio 1
	s_waitcnt lgkmcnt(0)
	v_mfma_scale_f32_16x16x128_f8f6f4 v[152:155], v[16:23], v[226:233], v[152:155], v189, v189 op_sel_hi:[0,0,0]
	v_mfma_scale_f32_16x16x128_f8f6f4 v[144:147], v[24:31], v[226:233], v[144:147], v189, v189 op_sel_hi:[0,0,0]
	v_mfma_scale_f32_16x16x128_f8f6f4 v[136:139], v[16:23], v[234:241], v[136:139], v189, v189 op_sel_hi:[0,0,0]
	v_mfma_scale_f32_16x16x128_f8f6f4 v[128:131], v[24:31], v[234:241], v[128:131], v189, v189 op_sel_hi:[0,0,0]
	v_mfma_scale_f32_16x16x128_f8f6f4 v[120:123], v[16:23], v[242:249], v[120:123], v189, v189 op_sel_hi:[0,0,0]
	v_mfma_scale_f32_16x16x128_f8f6f4 v[112:115], v[24:31], v[242:249], v[112:115], v189, v189 op_sel_hi:[0,0,0]
	v_mfma_scale_f32_16x16x128_f8f6f4 v[104:107], v[16:23], v[204:211], v[104:107], v189, v189 op_sel_hi:[0,0,0]
	v_mfma_scale_f32_16x16x128_f8f6f4 v[96:99], v[24:31], v[204:211], v[96:99], v189, v189 op_sel_hi:[0,0,0]
	s_setprio 0
	s_mov_b32 m0, s44
	s_barrier
	ds_read_b128 v[204:207], v190 offset:16384
	ds_read_b128 v[226:229], v190 offset:18432
	ds_read_b128 v[208:211], v192 offset:16384
	ds_read_b128 v[230:233], v192 offset:18432
	ds_read_b128 v[234:237], v190 offset:20480
	ds_read_b128 v[242:245], v190 offset:22528
	ds_read_b128 v[238:241], v192 offset:20480
	ds_read_b128 v[246:249], v192 offset:22528
	global_load_lds_dwordx4 v186, s[26:27]
	s_mov_b32 m0, s50
	v_mov_b32_e32 v187, v173
	global_load_lds_dwordx4 v184, s[26:27]
	s_barrier
	s_waitcnt lgkmcnt(0)
	v_mov_b32_e32 v185, v173
	v_lshl_add_u64 v[186:187], s[26:27], 0, v[186:187]
	v_lshl_add_u64 v[184:185], s[26:27], 0, v[184:185]
	s_setprio 1
	s_waitcnt lgkmcnt(0)
	v_mfma_scale_f32_16x16x128_f8f6f4 v[92:95], v[0:7], v[204:211], v[92:95], v189, v189 op_sel_hi:[0,0,0]
	v_mfma_scale_f32_16x16x128_f8f6f4 v[84:87], v[8:15], v[204:211], v[84:87], v189, v189 op_sel_hi:[0,0,0]
	v_mfma_scale_f32_16x16x128_f8f6f4 v[76:79], v[0:7], v[226:233], v[76:79], v189, v189 op_sel_hi:[0,0,0]
	v_mfma_scale_f32_16x16x128_f8f6f4 v[68:71], v[8:15], v[226:233], v[68:71], v189, v189 op_sel_hi:[0,0,0]
	v_mfma_scale_f32_16x16x128_f8f6f4 v[60:63], v[0:7], v[234:241], v[60:63], v189, v189 op_sel_hi:[0,0,0]
	v_mfma_scale_f32_16x16x128_f8f6f4 v[52:55], v[8:15], v[234:241], v[52:55], v189, v189 op_sel_hi:[0,0,0]
	v_mfma_scale_f32_16x16x128_f8f6f4 v[44:47], v[0:7], v[242:249], v[44:47], v189, v189 op_sel_hi:[0,0,0]
	v_mfma_scale_f32_16x16x128_f8f6f4 v[36:39], v[8:15], v[242:249], v[36:39], v189, v189 op_sel_hi:[0,0,0]
	s_setprio 0
	s_barrier
	s_add_u32 s72, s24, 0x20000
	s_addc_u32 s73, s25, 0
	s_mov_b32 m0, s51
	v_lshl_add_u64 v[0:1], s[72:73], 0, v[160:161]
	global_load_lds_dwordx4 v[0:1], off
	v_lshl_add_u64 v[0:1], s[72:73], 0, v[162:163]
	s_mov_b32 m0, s56
	s_nop 0
	global_load_lds_dwordx4 v[0:1], off
	s_waitcnt vmcnt(6)
	s_barrier
	s_setprio 1
	v_mfma_scale_f32_16x16x128_f8f6f4 v[88:91], v[16:23], v[204:211], v[88:91], v189, v189 op_sel_hi:[0,0,0]
	v_mfma_scale_f32_16x16x128_f8f6f4 v[80:83], v[24:31], v[204:211], v[80:83], v189, v189 op_sel_hi:[0,0,0]
	v_mfma_scale_f32_16x16x128_f8f6f4 v[72:75], v[16:23], v[226:233], v[72:75], v189, v189 op_sel_hi:[0,0,0]
	v_mfma_scale_f32_16x16x128_f8f6f4 v[64:67], v[24:31], v[226:233], v[64:67], v189, v189 op_sel_hi:[0,0,0]
	v_mfma_scale_f32_16x16x128_f8f6f4 v[56:59], v[16:23], v[234:241], v[56:59], v189, v189 op_sel_hi:[0,0,0]
	v_mfma_scale_f32_16x16x128_f8f6f4 v[48:51], v[24:31], v[234:241], v[48:51], v189, v189 op_sel_hi:[0,0,0]
	v_mfma_scale_f32_16x16x128_f8f6f4 v[40:43], v[16:23], v[242:249], v[40:43], v189, v189 op_sel_hi:[0,0,0]
	v_mfma_scale_f32_16x16x128_f8f6f4 v[32:35], v[24:31], v[242:249], v[32:35], v189, v189 op_sel_hi:[0,0,0]
	s_setprio 0
	s_barrier
	ds_read_b128 v[0:3], v191 offset:32768
	ds_read_b128 v[8:11], v191 offset:34816
	ds_read_b128 v[4:7], v193 offset:32768
	ds_read_b128 v[12:15], v193 offset:34816
	s_mov_b32 m0, s65
	v_lshl_add_u64 v[178:179], s[26:27], 0, v[178:179]
	ds_read_b128 v[16:19], v190 offset:32768
	ds_read_b128 v[24:27], v190 offset:34816
	ds_read_b128 v[20:23], v192 offset:32768
	ds_read_b128 v[28:31], v192 offset:34816
	ds_read_b128 v[204:207], v190 offset:36864
	ds_read_b128 v[226:229], v190 offset:38912
	ds_read_b128 v[208:211], v192 offset:36864
	ds_read_b128 v[230:233], v192 offset:38912
	global_load_lds_dwordx4 v[178:179], off
	v_lshl_add_u64 v[176:177], s[26:27], 0, v[176:177]
	s_mov_b32 m0, s70
	s_nop 0
	global_load_lds_dwordx4 v[176:177], off
	s_waitcnt lgkmcnt(8)
	s_barrier
	s_waitcnt lgkmcnt(0)
	s_setprio 1
	s_waitcnt lgkmcnt(0)
	v_mfma_scale_f32_16x16x128_f8f6f4 v[156:159], v[0:7], v[16:23], v[156:159], v189, v189 op_sel_hi:[0,0,0]
	v_mfma_scale_f32_16x16x128_f8f6f4 v[148:151], v[8:15], v[16:23], v[148:151], v189, v189 op_sel_hi:[0,0,0]
	v_mfma_scale_f32_16x16x128_f8f6f4 v[140:143], v[0:7], v[24:31], v[140:143], v189, v189 op_sel_hi:[0,0,0]
	v_mfma_scale_f32_16x16x128_f8f6f4 v[132:135], v[8:15], v[24:31], v[132:135], v189, v189 op_sel_hi:[0,0,0]
	v_mfma_scale_f32_16x16x128_f8f6f4 v[124:127], v[0:7], v[204:211], v[124:127], v189, v189 op_sel_hi:[0,0,0]
	v_mfma_scale_f32_16x16x128_f8f6f4 v[116:119], v[8:15], v[204:211], v[116:119], v189, v189 op_sel_hi:[0,0,0]
	v_mfma_scale_f32_16x16x128_f8f6f4 v[108:111], v[0:7], v[226:233], v[108:111], v189, v189 op_sel_hi:[0,0,0]
	v_mfma_scale_f32_16x16x128_f8f6f4 v[100:103], v[8:15], v[226:233], v[100:103], v189, v189 op_sel_hi:[0,0,0]
	s_setprio 0
	s_barrier
	s_mov_b32 m0, s71
	v_lshl_add_u64 v[176:177], v[180:181], 0, s[40:41]
	ds_read_b128 v[234:237], v191 offset:49152
	ds_read_b128 v[242:245], v191 offset:51200
	ds_read_b128 v[238:241], v193 offset:49152
	ds_read_b128 v[246:249], v193 offset:51200
	global_load_lds_dwordx4 v[176:177], off
	v_lshl_add_u64 v[176:177], v[182:183], 0, s[40:41]
	s_mov_b32 m0, s80
	s_nop 0
	global_load_lds_dwordx4 v[176:177], off
	s_barrier
	s_waitcnt lgkmcnt(0)
	s_setprio 1
	s_waitcnt lgkmcnt(0)
	v_mfma_scale_f32_16x16x128_f8f6f4 v[152:155], v[234:241], v[16:23], v[152:155], v189, v189 op_sel_hi:[0,0,0]
	v_mfma_scale_f32_16x16x128_f8f6f4 v[144:147], v[242:249], v[16:23], v[144:147], v189, v189 op_sel_hi:[0,0,0]
	v_mfma_scale_f32_16x16x128_f8f6f4 v[136:139], v[234:241], v[24:31], v[136:139], v189, v189 op_sel_hi:[0,0,0]
	v_mfma_scale_f32_16x16x128_f8f6f4 v[128:131], v[242:249], v[24:31], v[128:131], v189, v189 op_sel_hi:[0,0,0]
	v_mfma_scale_f32_16x16x128_f8f6f4 v[120:123], v[234:241], v[204:211], v[120:123], v189, v189 op_sel_hi:[0,0,0]
	v_mfma_scale_f32_16x16x128_f8f6f4 v[112:115], v[242:249], v[204:211], v[112:115], v189, v189 op_sel_hi:[0,0,0]
	v_mfma_scale_f32_16x16x128_f8f6f4 v[104:107], v[234:241], v[226:233], v[104:107], v189, v189 op_sel_hi:[0,0,0]
	v_mfma_scale_f32_16x16x128_f8f6f4 v[96:99], v[242:249], v[226:233], v[96:99], v189, v189 op_sel_hi:[0,0,0]
	s_setprio 0
	s_mov_b32 m0, s81
	v_lshl_add_u64 v[186:187], v[186:187], 0, s[40:41]
	s_barrier
	ds_read_b128 v[16:19], v190 offset:49152
	ds_read_b128 v[24:27], v190 offset:51200
	ds_read_b128 v[20:23], v192 offset:49152
	ds_read_b128 v[28:31], v192 offset:51200
	ds_read_b128 v[176:179], v190 offset:53248
	ds_read_b128 v[204:207], v190 offset:55296
	ds_read_b128 v[180:183], v192 offset:53248
	ds_read_b128 v[208:211], v192 offset:55296
	global_load_lds_dwordx4 v[186:187], off
	v_lshl_add_u64 v[184:185], v[184:185], 0, s[40:41]
	s_mov_b32 m0, s82
	s_nop 0
	global_load_lds_dwordx4 v[184:185], off
	s_barrier
	s_waitcnt lgkmcnt(0)
	s_setprio 1
	s_waitcnt lgkmcnt(0)
	v_mfma_scale_f32_16x16x128_f8f6f4 v[92:95], v[0:7], v[16:23], v[92:95], v189, v189 op_sel_hi:[0,0,0]
	v_mfma_scale_f32_16x16x128_f8f6f4 v[84:87], v[8:15], v[16:23], v[84:87], v189, v189 op_sel_hi:[0,0,0]
	v_mfma_scale_f32_16x16x128_f8f6f4 v[76:79], v[0:7], v[24:31], v[76:79], v189, v189 op_sel_hi:[0,0,0]
	v_mfma_scale_f32_16x16x128_f8f6f4 v[68:71], v[8:15], v[24:31], v[68:71], v189, v189 op_sel_hi:[0,0,0]
	v_mfma_scale_f32_16x16x128_f8f6f4 v[60:63], v[0:7], v[176:183], v[60:63], v189, v189 op_sel_hi:[0,0,0]
	v_mfma_scale_f32_16x16x128_f8f6f4 v[52:55], v[8:15], v[176:183], v[52:55], v189, v189 op_sel_hi:[0,0,0]
	v_mfma_scale_f32_16x16x128_f8f6f4 v[44:47], v[0:7], v[204:211], v[44:47], v189, v189 op_sel_hi:[0,0,0]
	v_mfma_scale_f32_16x16x128_f8f6f4 v[36:39], v[8:15], v[204:211], v[36:39], v189, v189 op_sel_hi:[0,0,0]
	s_setprio 0
	s_barrier
	s_add_u32 s24, s24, 0x20080
	s_addc_u32 s25, s25, 0
	s_mov_b32 m0, s83
	v_lshl_add_u64 v[0:1], s[24:25], 0, v[160:161]
	global_load_lds_dwordx4 v[0:1], off
	v_lshl_add_u64 v[0:1], s[24:25], 0, v[162:163]
	s_mov_b32 m0, s85
	s_nop 0
	global_load_lds_dwordx4 v[0:1], off
	s_waitcnt vmcnt(6)
	s_barrier
	s_setprio 1
	v_mfma_scale_f32_16x16x128_f8f6f4 v[88:91], v[234:241], v[16:23], v[88:91], v189, v189 op_sel_hi:[0,0,0]
	v_mfma_scale_f32_16x16x128_f8f6f4 v[80:83], v[242:249], v[16:23], v[80:83], v189, v189 op_sel_hi:[0,0,0]
	v_mfma_scale_f32_16x16x128_f8f6f4 v[72:75], v[234:241], v[24:31], v[72:75], v189, v189 op_sel_hi:[0,0,0]
	v_mfma_scale_f32_16x16x128_f8f6f4 v[64:67], v[242:249], v[24:31], v[64:67], v189, v189 op_sel_hi:[0,0,0]
	v_mfma_scale_f32_16x16x128_f8f6f4 v[56:59], v[234:241], v[176:183], v[56:59], v189, v189 op_sel_hi:[0,0,0]
	v_mfma_scale_f32_16x16x128_f8f6f4 v[48:51], v[242:249], v[176:183], v[48:51], v189, v189 op_sel_hi:[0,0,0]
	v_mfma_scale_f32_16x16x128_f8f6f4 v[40:43], v[234:241], v[204:211], v[40:43], v189, v189 op_sel_hi:[0,0,0]
	v_mfma_scale_f32_16x16x128_f8f6f4 v[32:35], v[242:249], v[204:211], v[32:35], v189, v189 op_sel_hi:[0,0,0]
	s_setprio 0
	s_add_i32 s64, s64, 2
	s_add_u32 s22, s22, 0x100
	s_addc_u32 s23, s23, 0
	s_add_u32 s2, s2, 0x100
	s_addc_u32 s3, s3, 0
	s_cmp_gt_u32 s64, 5
	s_cbranch_scc1 .Lrot_exit_3
	s_cmp_eq_u32 s64, 4
	s_cselect_b64 s[24:25], -1, 0
	s_cmp_lg_u32 s64, 4
	s_cbranch_scc0 .Lrot_rare_3
	v_mov_b32_e32 v186, v166
	v_mov_b32_e32 v184, v170
	v_mov_b64_e32 v[178:179], v[168:169]
	v_mov_b64_e32 v[176:177], v[174:175]
	s_branch .Lrot_head_3

.Lrot_rarein_3:
	s_andn2_b64 vcc, exec, s[20:21]
	s_cbranch_vccnz .LBB0_1559
	v_mov_b32_e32 v0, v188
	s_nop 0
	v_ashrrev_i32_e32 v2, 31, v0
	v_lshrrev_b32_e32 v2, 26, v2
	v_lshlrev_b32_e32 v1, 4, v0
	v_add_u32_e32 v2, v0, v2
	v_bfe_i32 v0, v0, 27, 1
	v_lshrrev_b32_e32 v0, 22, v0
	v_add_u32_e32 v0, v1, v0
	v_and_b32_e32 v0, 0xfffffc00, v0
	v_sub_u32_e32 v0, v1, v0
	v_lshrrev_b32_e32 v3, 4, v0
	v_bitop3_b32 v0, v3, v0, 32 bitop3:0x6c
	v_ashrrev_i32_e32 v4, 31, v0
	v_lshrrev_b32_e32 v4, 26, v4
	v_add_u32_e32 v4, v0, v4
	v_ashrrev_i32_e32 v2, 6, v2
	v_ashrrev_i32_e32 v5, 6, v4
	v_and_b32_e32 v4, 0xc0, v4
	v_lshlrev_b32_e32 v3, 3, v2
	v_sub_u32_e32 v0, v0, v4
	v_and_b32_e32 v3, -16, v3
	v_lshlrev_b32_e32 v2, 5, v2
	v_ashrrev_i16_sdwa v0, v201, sext(v0) dst_sel:DWORD dst_unused:UNUSED_PAD src0_sel:DWORD src1_sel:BYTE_0
	v_add_u32_e32 v3, v5, v3
	v_and_b32_e32 v2, 32, v2
	v_bfe_i32 v0, v0, 0, 16
	v_add_lshl_u32 v0, v2, v0, 1
	v_lshlrev_b32_e32 v2, 10, v165
	v_cmp_lt_i32_e32 vcc, v3, v222
	s_nop 1
	v_cndmask_b32_e32 v2, 0, v2, vcc
	v_add_u32_e32 v215, v0, v2
	v_add_u32_e32 v2, 0x80, v3
	v_lshlrev_b32_e32 v3, 10, v221
	v_cmp_lt_i32_e32 vcc, v2, v222
	s_nop 1
	v_cndmask_b32_e32 v2, 0, v3, vcc
	v_add_u32_e32 v216, v0, v2
	v_add_u32_e32 v0, 0x2000, v1
	v_ashrrev_i32_e32 v1, 31, v0
	v_lshrrev_b32_e32 v1, 22, v1
	v_add_u32_e32 v1, v0, v1
	v_ashrrev_i32_e32 v1, 10, v1
	v_mul_i32_i24_e32 v2, 0x400, v1
	v_sub_u32_e32 v0, v0, v2
	v_lshrrev_b32_e32 v2, 4, v0
	v_bitop3_b32 v0, v2, v0, 32 bitop3:0x6c
	v_ashrrev_i32_e32 v3, 31, v0
	v_lshrrev_b32_e32 v3, 26, v3
	v_add_u32_e32 v3, v0, v3
	v_ashrrev_i32_e32 v4, 6, v3
	v_and_b32_e32 v3, 0xc0, v3
	v_lshlrev_b32_e32 v2, 3, v1
	v_sub_u32_e32 v0, v0, v3
	v_and_b32_e32 v2, -16, v2
	v_lshlrev_b32_e32 v1, 5, v1
	v_ashrrev_i16_sdwa v0, v201, sext(v0) dst_sel:DWORD dst_unused:UNUSED_PAD src0_sel:DWORD src1_sel:BYTE_0
	v_add_u32_e32 v2, v4, v2
	v_and_b32_e32 v1, 32, v1
	v_bfe_i32 v0, v0, 0, 16
	v_add_lshl_u32 v0, v1, v0, 1
	v_lshlrev_b32_e32 v1, 10, v223
	v_cmp_lt_i32_e32 vcc, v2, v222
	s_nop 1
	v_cndmask_b32_e32 v1, 0, v1, vcc
	v_add_u32_e32 v217, v0, v1
	v_add_u32_e32 v1, 0x80, v2
	v_lshlrev_b32_e32 v2, 10, v224
	v_cmp_lt_i32_e32 vcc, v1, v222
	s_nop 1
	v_cndmask_b32_e32 v1, 0, v2, vcc
	v_add_u32_e32 v218, v0, v1

.LBB0_1666:
	ds_read_b128 v[0:3], v190
	ds_read_b128 v[8:11], v190 offset:2048
	ds_read_b128 v[4:7], v192
	ds_read_b128 v[12:15], v192 offset:2048
	s_add_u32 s26, s22, 0x80
	s_addc_u32 s27, s23, 0
	s_and_b64 s[24:25], s[24:25], exec
	s_cselect_b32 s27, s19, s27
	s_cselect_b32 s26, s18, s26
	s_cselect_b32 s25, s17, s83
	s_cselect_b32 s24, s16, s7
	v_lshl_add_u64 v[16:17], s[22:23], 0, v[166:167]
	s_add_i32 m0, s13, 0xc000
	ds_read_b128 v[204:207], v189
	ds_read_b128 v[216:219], v189 offset:2048
	ds_read_b128 v[208:211], v191
	ds_read_b128 v[220:223], v191 offset:2048
	ds_read_b128 v[224:227], v189 offset:4096
	ds_read_b128 v[232:235], v189 offset:6144
	ds_read_b128 v[228:231], v191 offset:4096
	ds_read_b128 v[236:239], v191 offset:6144
	global_load_lds_dwordx4 v[16:17], off
	v_lshl_add_u64 v[16:17], s[22:23], 0, v[170:171]
	s_add_i32 m0, s13, 0xe000
	s_nop 0
	global_load_lds_dwordx4 v[16:17], off
	s_waitcnt lgkmcnt(8)
	s_barrier
	s_waitcnt lgkmcnt(0)
	s_setprio 1
	s_waitcnt lgkmcnt(0)
	v_mfma_scale_f32_16x16x128_f8f6f4 v[156:159], v[0:7], v[204:211], v[156:159], v188, v188 op_sel_hi:[0,0,0]
	v_mfma_scale_f32_16x16x128_f8f6f4 v[152:155], v[8:15], v[204:211], v[152:155], v188, v188 op_sel_hi:[0,0,0]
	v_mfma_scale_f32_16x16x128_f8f6f4 v[148:151], v[0:7], v[216:223], v[148:151], v188, v188 op_sel_hi:[0,0,0]
	v_mfma_scale_f32_16x16x128_f8f6f4 v[144:147], v[8:15], v[216:223], v[144:147], v188, v188 op_sel_hi:[0,0,0]
	v_mfma_scale_f32_16x16x128_f8f6f4 v[140:143], v[0:7], v[224:231], v[140:143], v188, v188 op_sel_hi:[0,0,0]
	v_mfma_scale_f32_16x16x128_f8f6f4 v[136:139], v[8:15], v[224:231], v[136:139], v188, v188 op_sel_hi:[0,0,0]
	v_mfma_scale_f32_16x16x128_f8f6f4 v[132:135], v[0:7], v[232:239], v[132:135], v188, v188 op_sel_hi:[0,0,0]
	v_mfma_scale_f32_16x16x128_f8f6f4 v[128:131], v[8:15], v[232:239], v[128:131], v188, v188 op_sel_hi:[0,0,0]
	s_setprio 0
	s_barrier
	s_mov_b32 m0, s15
	v_lshl_add_u64 v[180:181], s[24:25], 0, v[162:163]
	ds_read_b128 v[16:19], v190 offset:16384
	ds_read_b128 v[24:27], v190 offset:18432
	ds_read_b128 v[20:23], v192 offset:16384
	ds_read_b128 v[28:31], v192 offset:18432
	global_load_lds_dwordx4 v[180:181], off
	v_lshl_add_u64 v[182:183], s[24:25], 0, v[164:165]
	s_mov_b32 m0, s31
	s_nop 0
	global_load_lds_dwordx4 v[182:183], off
	s_barrier
	s_waitcnt lgkmcnt(0)
	s_setprio 1
	s_waitcnt lgkmcnt(0)
	v_mfma_scale_f32_16x16x128_f8f6f4 v[100:103], v[16:23], v[204:211], v[100:103], v188, v188 op_sel_hi:[0,0,0]
	v_mfma_scale_f32_16x16x128_f8f6f4 v[96:99], v[24:31], v[204:211], v[96:99], v188, v188 op_sel_hi:[0,0,0]
	v_mfma_scale_f32_16x16x128_f8f6f4 v[84:87], v[16:23], v[216:223], v[84:87], v188, v188 op_sel_hi:[0,0,0]
	v_mfma_scale_f32_16x16x128_f8f6f4 v[80:83], v[24:31], v[216:223], v[80:83], v188, v188 op_sel_hi:[0,0,0]
	v_mfma_scale_f32_16x16x128_f8f6f4 v[76:79], v[16:23], v[224:231], v[76:79], v188, v188 op_sel_hi:[0,0,0]
	v_mfma_scale_f32_16x16x128_f8f6f4 v[72:75], v[24:31], v[224:231], v[72:75], v188, v188 op_sel_hi:[0,0,0]
	v_mfma_scale_f32_16x16x128_f8f6f4 v[68:71], v[16:23], v[232:239], v[68:71], v188, v188 op_sel_hi:[0,0,0]
	v_mfma_scale_f32_16x16x128_f8f6f4 v[64:67], v[24:31], v[232:239], v[64:67], v188, v188 op_sel_hi:[0,0,0]
	s_setprio 0
	s_mov_b32 m0, s13
	s_barrier
	ds_read_b128 v[204:207], v189 offset:16384
	ds_read_b128 v[216:219], v189 offset:18432
	ds_read_b128 v[208:211], v191 offset:16384
	ds_read_b128 v[220:223], v191 offset:18432
	ds_read_b128 v[224:227], v189 offset:20480
	ds_read_b128 v[232:235], v189 offset:22528
	ds_read_b128 v[228:231], v191 offset:20480
	ds_read_b128 v[236:239], v191 offset:22528
	global_load_lds_dwordx4 v172, s[26:27]
	s_mov_b32 m0, s44
	v_mov_b32_e32 v185, v173
	global_load_lds_dwordx4 v184, s[26:27]
	s_barrier
	s_waitcnt lgkmcnt(0)
	v_lshl_add_u64 v[186:187], s[26:27], 0, v[172:173]
	v_lshl_add_u64 v[184:185], s[26:27], 0, v[184:185]
	s_setprio 1
	s_waitcnt lgkmcnt(0)
	v_mfma_scale_f32_16x16x128_f8f6f4 v[124:127], v[0:7], v[204:211], v[124:127], v188, v188 op_sel_hi:[0,0,0]
	v_mfma_scale_f32_16x16x128_f8f6f4 v[120:123], v[8:15], v[204:211], v[120:123], v188, v188 op_sel_hi:[0,0,0]
	v_mfma_scale_f32_16x16x128_f8f6f4 v[116:119], v[0:7], v[216:223], v[116:119], v188, v188 op_sel_hi:[0,0,0]
	v_mfma_scale_f32_16x16x128_f8f6f4 v[112:115], v[8:15], v[216:223], v[112:115], v188, v188 op_sel_hi:[0,0,0]
	v_mfma_scale_f32_16x16x128_f8f6f4 v[108:111], v[0:7], v[224:231], v[108:111], v188, v188 op_sel_hi:[0,0,0]
	v_mfma_scale_f32_16x16x128_f8f6f4 v[104:107], v[8:15], v[224:231], v[104:107], v188, v188 op_sel_hi:[0,0,0]
	v_mfma_scale_f32_16x16x128_f8f6f4 v[92:95], v[0:7], v[232:239], v[92:95], v188, v188 op_sel_hi:[0,0,0]
	v_mfma_scale_f32_16x16x128_f8f6f4 v[88:91], v[8:15], v[232:239], v[88:91], v188, v188 op_sel_hi:[0,0,0]
	s_setprio 0
	s_barrier
	s_add_u32 s90, s24, 0x20000
	s_addc_u32 s91, s25, 0
	s_mov_b32 m0, s46
	v_lshl_add_u64 v[0:1], s[90:91], 0, v[162:163]
	global_load_lds_dwordx4 v[0:1], off
	v_lshl_add_u64 v[0:1], s[90:91], 0, v[164:165]
	s_mov_b32 m0, s47
	s_nop 0
	global_load_lds_dwordx4 v[0:1], off
	s_waitcnt vmcnt(6)
	s_barrier
	s_setprio 1
	v_mfma_scale_f32_16x16x128_f8f6f4 v[60:63], v[16:23], v[204:211], v[60:63], v188, v188 op_sel_hi:[0,0,0]
	v_mfma_scale_f32_16x16x128_f8f6f4 v[56:59], v[24:31], v[204:211], v[56:59], v188, v188 op_sel_hi:[0,0,0]
	v_mfma_scale_f32_16x16x128_f8f6f4 v[52:55], v[16:23], v[216:223], v[52:55], v188, v188 op_sel_hi:[0,0,0]
	v_mfma_scale_f32_16x16x128_f8f6f4 v[48:51], v[24:31], v[216:223], v[48:51], v188, v188 op_sel_hi:[0,0,0]
	v_mfma_scale_f32_16x16x128_f8f6f4 v[44:47], v[16:23], v[224:231], v[44:47], v188, v188 op_sel_hi:[0,0,0]
	v_mfma_scale_f32_16x16x128_f8f6f4 v[40:43], v[24:31], v[224:231], v[40:43], v188, v188 op_sel_hi:[0,0,0]
	v_mfma_scale_f32_16x16x128_f8f6f4 v[36:39], v[16:23], v[232:239], v[36:39], v188, v188 op_sel_hi:[0,0,0]
	v_mfma_scale_f32_16x16x128_f8f6f4 v[32:35], v[24:31], v[232:239], v[32:35], v188, v188 op_sel_hi:[0,0,0]
	s_setprio 0
	s_barrier
	ds_read_b128 v[0:3], v190 offset:32768
	ds_read_b128 v[8:11], v190 offset:34816
	ds_read_b128 v[4:7], v192 offset:32768
	ds_read_b128 v[12:15], v192 offset:34816
	s_mov_b32 m0, s50
	v_lshl_add_u64 v[178:179], s[26:27], 0, v[178:179]
	ds_read_b128 v[16:19], v189 offset:32768
	ds_read_b128 v[24:27], v189 offset:34816
	ds_read_b128 v[20:23], v191 offset:32768
	ds_read_b128 v[28:31], v191 offset:34816
	ds_read_b128 v[204:207], v189 offset:36864
	ds_read_b128 v[216:219], v189 offset:38912
	ds_read_b128 v[208:211], v191 offset:36864
	ds_read_b128 v[220:223], v191 offset:38912
	global_load_lds_dwordx4 v[178:179], off
	v_lshl_add_u64 v[176:177], s[26:27], 0, v[176:177]
	s_mov_b32 m0, s51
	s_nop 0
	global_load_lds_dwordx4 v[176:177], off
	s_waitcnt lgkmcnt(8)
	s_barrier
	s_waitcnt lgkmcnt(0)
	s_setprio 1
	s_waitcnt lgkmcnt(0)
	v_mfma_scale_f32_16x16x128_f8f6f4 v[156:159], v[0:7], v[16:23], v[156:159], v188, v188 op_sel_hi:[0,0,0]
	v_mfma_scale_f32_16x16x128_f8f6f4 v[152:155], v[8:15], v[16:23], v[152:155], v188, v188 op_sel_hi:[0,0,0]
	v_mfma_scale_f32_16x16x128_f8f6f4 v[148:151], v[0:7], v[24:31], v[148:151], v188, v188 op_sel_hi:[0,0,0]
	v_mfma_scale_f32_16x16x128_f8f6f4 v[144:147], v[8:15], v[24:31], v[144:147], v188, v188 op_sel_hi:[0,0,0]
	v_mfma_scale_f32_16x16x128_f8f6f4 v[140:143], v[0:7], v[204:211], v[140:143], v188, v188 op_sel_hi:[0,0,0]
	v_mfma_scale_f32_16x16x128_f8f6f4 v[136:139], v[8:15], v[204:211], v[136:139], v188, v188 op_sel_hi:[0,0,0]
	v_mfma_scale_f32_16x16x128_f8f6f4 v[132:135], v[0:7], v[216:223], v[132:135], v188, v188 op_sel_hi:[0,0,0]
	v_mfma_scale_f32_16x16x128_f8f6f4 v[128:131], v[8:15], v[216:223], v[128:131], v188, v188 op_sel_hi:[0,0,0]
	s_setprio 0
	s_barrier
	s_mov_b32 m0, s56
	v_lshl_add_u64 v[176:177], v[180:181], 0, s[40:41]
	ds_read_b128 v[224:227], v190 offset:49152
	ds_read_b128 v[232:235], v190 offset:51200
	ds_read_b128 v[228:231], v192 offset:49152
	ds_read_b128 v[236:239], v192 offset:51200
	global_load_lds_dwordx4 v[176:177], off
	v_lshl_add_u64 v[176:177], v[182:183], 0, s[40:41]
	s_mov_b32 m0, s57
	s_nop 0
	global_load_lds_dwordx4 v[176:177], off
	s_barrier
	s_waitcnt lgkmcnt(0)
	s_setprio 1
	s_waitcnt lgkmcnt(0)
	v_mfma_scale_f32_16x16x128_f8f6f4 v[100:103], v[224:231], v[16:23], v[100:103], v188, v188 op_sel_hi:[0,0,0]
	v_mfma_scale_f32_16x16x128_f8f6f4 v[96:99], v[232:239], v[16:23], v[96:99], v188, v188 op_sel_hi:[0,0,0]
	v_mfma_scale_f32_16x16x128_f8f6f4 v[84:87], v[224:231], v[24:31], v[84:87], v188, v188 op_sel_hi:[0,0,0]
	v_mfma_scale_f32_16x16x128_f8f6f4 v[80:83], v[232:239], v[24:31], v[80:83], v188, v188 op_sel_hi:[0,0,0]
	v_mfma_scale_f32_16x16x128_f8f6f4 v[76:79], v[224:231], v[204:211], v[76:79], v188, v188 op_sel_hi:[0,0,0]
	v_mfma_scale_f32_16x16x128_f8f6f4 v[72:75], v[232:239], v[204:211], v[72:75], v188, v188 op_sel_hi:[0,0,0]
	v_mfma_scale_f32_16x16x128_f8f6f4 v[68:71], v[224:231], v[216:223], v[68:71], v188, v188 op_sel_hi:[0,0,0]
	v_mfma_scale_f32_16x16x128_f8f6f4 v[64:67], v[232:239], v[216:223], v[64:67], v188, v188 op_sel_hi:[0,0,0]
	s_setprio 0
	s_mov_b32 m0, s64
	v_lshl_add_u64 v[186:187], v[186:187], 0, s[40:41]
	s_barrier
	ds_read_b128 v[16:19], v189 offset:49152
	ds_read_b128 v[24:27], v189 offset:51200
	ds_read_b128 v[20:23], v191 offset:49152
	ds_read_b128 v[28:31], v191 offset:51200
	ds_read_b128 v[176:179], v189 offset:53248
	ds_read_b128 v[204:207], v189 offset:55296
	ds_read_b128 v[180:183], v191 offset:53248
	ds_read_b128 v[208:211], v191 offset:55296
	global_load_lds_dwordx4 v[186:187], off
	v_lshl_add_u64 v[184:185], v[184:185], 0, s[40:41]
	s_mov_b32 m0, s65
	s_nop 0
	global_load_lds_dwordx4 v[184:185], off
	s_barrier
	s_waitcnt lgkmcnt(0)
	s_setprio 1
	s_waitcnt lgkmcnt(0)
	v_mfma_scale_f32_16x16x128_f8f6f4 v[124:127], v[0:7], v[16:23], v[124:127], v188, v188 op_sel_hi:[0,0,0]
	v_mfma_scale_f32_16x16x128_f8f6f4 v[120:123], v[8:15], v[16:23], v[120:123], v188, v188 op_sel_hi:[0,0,0]
	v_mfma_scale_f32_16x16x128_f8f6f4 v[116:119], v[0:7], v[24:31], v[116:119], v188, v188 op_sel_hi:[0,0,0]
	v_mfma_scale_f32_16x16x128_f8f6f4 v[112:115], v[8:15], v[24:31], v[112:115], v188, v188 op_sel_hi:[0,0,0]
	v_mfma_scale_f32_16x16x128_f8f6f4 v[108:111], v[0:7], v[176:183], v[108:111], v188, v188 op_sel_hi:[0,0,0]
	v_mfma_scale_f32_16x16x128_f8f6f4 v[104:107], v[8:15], v[176:183], v[104:107], v188, v188 op_sel_hi:[0,0,0]
	v_mfma_scale_f32_16x16x128_f8f6f4 v[92:95], v[0:7], v[204:211], v[92:95], v188, v188 op_sel_hi:[0,0,0]
	v_mfma_scale_f32_16x16x128_f8f6f4 v[88:91], v[8:15], v[204:211], v[88:91], v188, v188 op_sel_hi:[0,0,0]
	s_setprio 0
	s_barrier
	s_add_u32 s24, s24, 0x20080
	s_addc_u32 s25, s25, 0
	s_mov_b32 m0, s70
	v_lshl_add_u64 v[0:1], s[24:25], 0, v[162:163]
	global_load_lds_dwordx4 v[0:1], off
	v_lshl_add_u64 v[0:1], s[24:25], 0, v[164:165]
	s_mov_b32 m0, s71
	s_nop 0
	global_load_lds_dwordx4 v[0:1], off
	s_waitcnt vmcnt(6)
	s_barrier
	s_setprio 1
	v_mfma_scale_f32_16x16x128_f8f6f4 v[60:63], v[224:231], v[16:23], v[60:63], v188, v188 op_sel_hi:[0,0,0]
	v_mfma_scale_f32_16x16x128_f8f6f4 v[56:59], v[232:239], v[16:23], v[56:59], v188, v188 op_sel_hi:[0,0,0]
	v_mfma_scale_f32_16x16x128_f8f6f4 v[52:55], v[224:231], v[24:31], v[52:55], v188, v188 op_sel_hi:[0,0,0]
	v_mfma_scale_f32_16x16x128_f8f6f4 v[48:51], v[232:239], v[24:31], v[48:51], v188, v188 op_sel_hi:[0,0,0]
	v_mfma_scale_f32_16x16x128_f8f6f4 v[44:47], v[224:231], v[176:183], v[44:47], v188, v188 op_sel_hi:[0,0,0]
	v_mfma_scale_f32_16x16x128_f8f6f4 v[40:43], v[232:239], v[176:183], v[40:43], v188, v188 op_sel_hi:[0,0,0]
	v_mfma_scale_f32_16x16x128_f8f6f4 v[36:39], v[224:231], v[204:211], v[36:39], v188, v188 op_sel_hi:[0,0,0]
	v_mfma_scale_f32_16x16x128_f8f6f4 v[32:35], v[232:239], v[204:211], v[32:35], v188, v188 op_sel_hi:[0,0,0]
	s_setprio 0
	s_add_i32 s85, s85, 2
	s_add_u32 s22, s22, 0x100
	s_addc_u32 s23, s23, 0
	s_add_u32 s7, s7, 0x100
	s_addc_u32 s83, s83, 0
	s_cmp_gt_u32 s85, 5
	s_cbranch_scc1 .Lrot_exit_2
	s_cmp_eq_u32 s85, 4
	s_cselect_b64 s[24:25], -1, 0
	s_cmp_lg_u32 s85, 4
	v_mov_b64_e32 v[176:177], v[170:171]
	v_mov_b64_e32 v[178:179], v[166:167]
	v_mov_b32_e32 v184, v174
	v_mov_b32_e32 v172, v168
	s_cbranch_scc1 .Lrot_head_2
	v_mov_b32_e32 v0, v195
	v_mov_b32_e32 v172, v196
	v_mov_b32_e32 v184, v197
	v_mov_b32_e32 v176, v214
	v_mov_b32_e32 v177, v173
	v_mov_b64_e32 v[178:179], v[172:173]
	v_mov_b32_e32 v172, v0
	s_branch .Lrot_head_2
